# v39 + anti-phased sectional priority in the MLA steady loops: s_setprio 1 while a wave is in its QK section, 0 in its PV section
# baseline (speedup 1.0000x reference)
; template <bool FOX>
; __device__ __forceinline__ void attn_unit(const Args& A, int b, int h, int qb, LAS char* shm, LAS float* dg) {
;     ...
;     for (int t = 1; t < t_end; ++t) {
;         if (t == 1 && 4 < nti) ISSUE_K(t0 + 4, 0);
;         if (t + 4 < nti) ISSUE_K(t0 + t + 4, t % NS);
;         if (t + 2 < nti) ISSUE_V(t0 + t + 2, (t + 2) % NS);
;         SFENCE();
;         { if constexpr (!FOX) { if (t0 + t == tw_last + 1) {
; #pragma unroll
;                   for (int r = 0; r < 16; ++r) negm[r] = -INFINITY;
;                   asm volatile("" : "+v"(negm)); } }
;           const lds_cptr vp = vp0 + ((t - 1) % NS) * VSLOT; float sa = 0.f, sb = 0.f;
; #pragma unroll
;           for (int g = 0; g < 2 * NQ; ++g) {
;               if (!FOX && g == 0) c0 = __builtin_amdgcn_mfma_f32_32x32x16_bf16(kf[0], qr[0], negm, 0, 0, 0);
;               else if (!FOX && g == 1) c1 = __builtin_amdgcn_mfma_f32_32x32x16_bf16(kf[1], qr[0], negm, 0, 0, 0);
;               else if (g & 1) c1 = __builtin_amdgcn_mfma_f32_32x32x16_bf16(kf[g], qr[g >> 1], c1, 0, 0, 0); else c0 = __builtin_amdgcn_mfma_f32_32x32x16_bf16(kf[g], qr[g >> 1], c0, 0, 0, 0);
;               if (g < 8) { const int i = (g >> 1) + 4 * (g & 1); vlo[i] = vtr(vp + (i >> 2) * 4096 + (i & 3) * 1024); vhi[i] = vtr(vp + (i >> 2) * 4096 + (i & 3) * 1024 + 512);
;                   if (g < 4) { sa += pp0[4 * g]; sb += pp0[4 * g + 1]; sa += pp0[4 * g + 2]; sb += pp0[4 * g + 3]; } else { sa += pp1[4 * g - 16]; sb += pp1[4 * g - 15]; sa += pp1[4 * g - 14]; sb += pp1[4 * g - 13]; }
;                   asm volatile("" : "+v"(sa), "+v"(sb)); }
;               { constexpr int G0 = FOX ? 0 : 4; if (g >= G0) { const int q = 2 * (g - G0);
; #pragma unroll
;                   for (int k = 0; k < 2; ++k) { const int w = q + k; const unsigned pkd = w < 8 ? cvt_pk_bf16(pp0[2 * w], pp0[2 * w + 1]) : cvt_pk_bf16(pp1[2 * w - 16], pp1[2 * w - 15]); pw[w >> 2][w & 3] = pkd; } } }
;               SFENCE();
;           }
;           lrun += sa + sb; }
;         MASKONLY(t);
;         float rm; ROWMAX(rm);
;         bool resc = false;
;         if (__any(rm > THR)) { const float dl = fmaxf(rm, 0.f); mhat += dl;
; #pragma unroll
;             for (int r = 0; r < 16; ++r) { c0[r] -= dl; c1[r] -= dl; }
;             if constexpr (!FOX) {
; #pragma unroll
;                 for (int r = 0; r < 16; ++r) negm[r] = -mhat;
.Lmla_ss1_in:
	s_mov_b32 m0, s52
	s_nop 0
	global_load_lds_dwordx4 v240, s[46:47]
	s_add_i32 m0, s52, 0x2000
	s_nop 0
	global_load_lds_dwordx4 v240, s[98:99]
	s_mov_b32 m0, s53
	s_nop 0
	global_load_lds_dwordx4 v240, s[60:61]
	s_waitcnt lgkmcnt(0)
	s_setprio 1
	s_add_i32 s27, s42, 0x8000
	v_mfma_f32_32x32x16_bf16 v[114:129], v[206:209], v[138:141], v[82:97]
	s_and_b32 s27, s27, 0x6000
	s_add_u32 s42, s42, 0x2000
	s_addc_u32 s43, s43, 0
	v_add_u32_e32 v3, s27, v247
	ds_read_b64_tr_b16 v[206:207], v3 offset:49152
	ds_read_b64_tr_b16 v[208:209], v3 offset:49664
	v_add_f32_e32 v4, v69, v67
	v_add_f32_e32 v5, v68, v66
	v_mfma_f32_32x32x16_bf16 v[98:113], v[194:197], v[138:141], v[82:97]
	ds_read_b64_tr_b16 v[194:195], v3 offset:53248
	ds_read_b64_tr_b16 v[196:197], v3 offset:53760
	v_add_f32_e32 v4, v71, v4
	v_add_f32_e32 v5, v70, v5
	v_add_f32_e32 v4, v73, v4
	v_add_f32_e32 v5, v72, v5
	v_mfma_f32_32x32x16_bf16 v[114:129], v[202:205], v[142:145], v[114:129]
	ds_read_b64_tr_b16 v[202:203], v3 offset:50176
	ds_read_b64_tr_b16 v[204:205], v3 offset:50688
	v_add_f32_e32 v4, v75, v4
	v_add_f32_e32 v5, v74, v5
	v_add_f32_e32 v4, v77, v4
	v_add_f32_e32 v5, v76, v5
	v_mfma_f32_32x32x16_bf16 v[98:113], v[186:189], v[142:145], v[98:113]
	ds_read_b64_tr_b16 v[214:215], v3 offset:54272
	ds_read_b64_tr_b16 v[216:217], v3 offset:54784
	v_add_f32_e32 v4, v79, v4
	v_add_f32_e32 v5, v78, v5
	v_add_f32_e32 v4, v81, v4
	v_add_f32_e32 v5, v80, v5
	v_mfma_f32_32x32x16_bf16 v[114:129], v[198:201], v[146:149], v[114:129]
	ds_read_b64_tr_b16 v[210:211], v3 offset:51200
	ds_read_b64_tr_b16 v[212:213], v3 offset:51712
	v_add_f32_e32 v4, v51, v4
	v_add_f32_e32 v5, v50, v5
	v_add_f32_e32 v4, v53, v4
	v_add_f32_e32 v5, v52, v5
	v_mfma_f32_32x32x16_bf16 v[98:113], v[182:185], v[146:149], v[98:113]
	ds_read_b64_tr_b16 v[12:13], v3 offset:55296
	ds_read_b64_tr_b16 v[14:15], v3 offset:55808
	v_add_f32_e32 v4, v55, v4
	v_add_f32_e32 v5, v54, v5
	v_add_f32_e32 v4, v57, v4
	v_add_f32_e32 v5, v56, v5
	v_mfma_f32_32x32x16_bf16 v[114:129], v[190:193], v[150:153], v[114:129]
	ds_read_b64_tr_b16 v[8:9], v3 offset:52224
	ds_read_b64_tr_b16 v[10:11], v3 offset:52736
	v_add_f32_e32 v4, v59, v4
	v_add_f32_e32 v16, v61, v4
	v_add_f32_e32 v4, v58, v5
	v_add_f32_e32 v17, v60, v4
	v_mfma_f32_32x32x16_bf16 v[98:113], v[170:173], v[150:153], v[98:113]
	s_add_u32 s46, s46, s62
	s_addc_u32 s47, s47, s63
	s_and_b32 s64, s26, 3
	ds_read_b64_tr_b16 v[4:5], v3 offset:56320
	ds_read_b64_tr_b16 v[6:7], v3 offset:56832
	v_add_f32_e32 v3, v63, v16
	v_add_f32_e32 v16, v62, v17
	v_add_f32_e32 v3, v65, v3
	v_add_f32_e32 v16, v64, v16
	v_mfma_f32_32x32x16_bf16 v[114:129], v[178:181], v[154:157], v[114:129]
	s_mulk_i32 s64, 0x3000
	s_add_u32 s60, s60, 0x2000
	s_addc_u32 s61, s61, 0
	v_cvt_pk_bf16_f32 v178, v50, v51
	v_cvt_pk_bf16_f32 v179, v52, v53
	v_cvt_pk_bf16_f32 v186, v66, v67
	v_cvt_pk_bf16_f32 v187, v68, v69
	v_mfma_f32_32x32x16_bf16 v[98:113], v[166:169], v[154:157], v[98:113]
	s_add_i32 s52, s64, s91
	s_add_i32 s64, s42, 0x6000
	s_add_u32 s98, s98, s62
	s_addc_u32 s99, s99, s63
	v_cvt_pk_bf16_f32 v180, v54, v55
	v_cvt_pk_bf16_f32 v181, v56, v57
	v_cvt_pk_bf16_f32 v188, v70, v71
	v_cvt_pk_bf16_f32 v189, v72, v73
	v_mfma_f32_32x32x16_bf16 v[114:129], v[174:177], v[158:161], v[114:129]
	s_and_b32 s64, s64, 0x6000
	s_add_i32 s53, s64, s93
	v_cvt_pk_bf16_f32 v218, v58, v59
	v_cvt_pk_bf16_f32 v219, v60, v61
	v_cvt_pk_bf16_f32 v182, v74, v75
	v_cvt_pk_bf16_f32 v183, v76, v77
	v_mfma_f32_32x32x16_bf16 v[98:113], v[162:165], v[158:161], v[98:113]
	v_cvt_pk_bf16_f32 v220, v62, v63
	v_cvt_pk_bf16_f32 v221, v64, v65
	v_cvt_pk_bf16_f32 v184, v78, v79
	v_cvt_pk_bf16_f32 v185, v80, v81
	v_add_f32_e32 v3, v3, v16
	v_add_f32_e32 v246, v246, v3
	s_nop 3
	s_waitcnt lgkmcnt(0)
	s_setprio 0
	v_mfma_f32_32x32x16_bf16 v[18:33], v[186:189], v[206:209], v[18:33]
	s_add_i32 s27, s26, 1
	s_and_b32 s64, s27, 3
	s_mulk_i32 s64, 0x3000
	v_exp_f32_e32 v66, v114
	v_exp_f32_e32 v67, v115
	v_exp_f32_e32 v68, v116
	v_exp_f32_e32 v69, v117
	v_add_u32_e32 v3, s64, v248
	v_mfma_f32_32x32x16_bf16 v[34:49], v[186:189], v[194:197], v[34:49]
	v_exp_f32_e32 v70, v118
	v_exp_f32_e32 v71, v119
	v_exp_f32_e32 v72, v120
	v_exp_f32_e32 v73, v121
	ds_read_b128 v[206:209], v3
	ds_read_b128 v[194:197], v3 offset:512
	v_mfma_f32_32x32x16_bf16 v[18:33], v[182:185], v[202:205], v[18:33]
	v_exp_f32_e32 v74, v122
	v_exp_f32_e32 v75, v123
	v_exp_f32_e32 v76, v124
	v_exp_f32_e32 v77, v125
	ds_read_b128 v[202:205], v3 offset:2048
	ds_read_b128 v[186:189], v3 offset:2560
	v_mfma_f32_32x32x16_bf16 v[34:49], v[182:185], v[214:217], v[34:49]
	v_exp_f32_e32 v78, v126
	v_exp_f32_e32 v79, v127
	v_exp_f32_e32 v80, v128
	v_exp_f32_e32 v81, v129
	ds_read_b128 v[198:201], v3 offset:4096
	ds_read_b128 v[182:185], v3 offset:4608
	v_mfma_f32_32x32x16_bf16 v[18:33], v[178:181], v[210:213], v[18:33]
	v_exp_f32_e32 v50, v98
	v_exp_f32_e32 v51, v99
	v_exp_f32_e32 v52, v100
	v_exp_f32_e32 v53, v101
	ds_read_b128 v[190:193], v3 offset:6144
	ds_read_b128 v[170:173], v3 offset:6656
	v_mfma_f32_32x32x16_bf16 v[34:49], v[178:181], v[12:15], v[34:49]
	v_exp_f32_e32 v54, v102
	v_exp_f32_e32 v55, v103
	v_exp_f32_e32 v56, v104
	v_exp_f32_e32 v57, v105
	ds_read_b128 v[178:181], v3 offset:8192
	ds_read_b128 v[166:169], v3 offset:8704
	v_mfma_f32_32x32x16_bf16 v[18:33], v[218:221], v[8:11], v[18:33]
	v_exp_f32_e32 v58, v106
	v_exp_f32_e32 v59, v107
	v_exp_f32_e32 v60, v108
	v_exp_f32_e32 v61, v109
	ds_read_b128 v[174:177], v3 offset:10240
	ds_read_b128 v[162:165], v3 offset:10752
	v_mfma_f32_32x32x16_bf16 v[34:49], v[218:221], v[4:7], v[34:49]
	v_exp_f32_e32 v62, v110
	v_exp_f32_e32 v63, v111
	v_exp_f32_e32 v64, v112
	v_exp_f32_e32 v65, v113
	s_mov_b32 s26, s27
	s_cmp_eq_u32 s27, s96
	s_cbranch_scc1 .Lmla_ss1_xdone
	s_add_i32 s64, s27, 3
	s_cmp_lt_u32 s64, s94
	s_cbranch_scc1 .Lmla_ss1_top
	s_waitcnt vmcnt(4)
	s_barrier
	s_branch .Lmla_ss_back

; template <bool FOX>
; __device__ __forceinline__ void attn_unit(const Args& A, int b, int h, int qb, LAS char* shm, LAS float* dg) {
;     ...
;     for (int t = 1; t < t_end; ++t) {
;         if (t == 1 && 4 < nti) ISSUE_K(t0 + 4, 0);
;         if (t + 4 < nti) ISSUE_K(t0 + t + 4, t % NS);
;         if (t + 2 < nti) ISSUE_V(t0 + t + 2, (t + 2) % NS);
;         SFENCE();
;         { if constexpr (!FOX) { if (t0 + t == tw_last + 1) {
; #pragma unroll
;                   for (int r = 0; r < 16; ++r) negm[r] = -INFINITY;
;                   asm volatile("" : "+v"(negm)); } }
;           const lds_cptr vp = vp0 + ((t - 1) % NS) * VSLOT; float sa = 0.f, sb = 0.f;
; #pragma unroll
;           for (int g = 0; g < 2 * NQ; ++g) {
;               if (!FOX && g == 0) c0 = __builtin_amdgcn_mfma_f32_32x32x16_bf16(kf[0], qr[0], negm, 0, 0, 0);
;               else if (!FOX && g == 1) c1 = __builtin_amdgcn_mfma_f32_32x32x16_bf16(kf[1], qr[0], negm, 0, 0, 0);
;               else if (g & 1) c1 = __builtin_amdgcn_mfma_f32_32x32x16_bf16(kf[g], qr[g >> 1], c1, 0, 0, 0); else c0 = __builtin_amdgcn_mfma_f32_32x32x16_bf16(kf[g], qr[g >> 1], c0, 0, 0, 0);
;               if (g < 8) { const int i = (g >> 1) + 4 * (g & 1); vlo[i] = vtr(vp + (i >> 2) * 4096 + (i & 3) * 1024); vhi[i] = vtr(vp + (i >> 2) * 4096 + (i & 3) * 1024 + 512);
;                   if (g < 4) { sa += pp0[4 * g]; sb += pp0[4 * g + 1]; sa += pp0[4 * g + 2]; sb += pp0[4 * g + 3]; } else { sa += pp1[4 * g - 16]; sb += pp1[4 * g - 15]; sa += pp1[4 * g - 14]; sb += pp1[4 * g - 13]; }
;                   asm volatile("" : "+v"(sa), "+v"(sb)); }
;               { constexpr int G0 = FOX ? 0 : 4; if (g >= G0) { const int q = 2 * (g - G0);
; #pragma unroll
;                   for (int k = 0; k < 2; ++k) { const int w = q + k; const unsigned pkd = w < 8 ? cvt_pk_bf16(pp0[2 * w], pp0[2 * w + 1]) : cvt_pk_bf16(pp1[2 * w - 16], pp1[2 * w - 15]); pw[w >> 2][w & 3] = pkd; } } }
;               SFENCE();
;           }
;           lrun += sa + sb; }
;         MASKONLY(t);
;         float rm; ROWMAX(rm);
;         bool resc = false;
;         if (__any(rm > THR)) { const float dl = fmaxf(rm, 0.f); mhat += dl;
; #pragma unroll
;             for (int r = 0; r < 16; ++r) { c0[r] -= dl; c1[r] -= dl; }
;             if constexpr (!FOX) {
; #pragma unroll
;                 for (int r = 0; r < 16; ++r) negm[r] = -mhat;
.Lmla_ss2_top:
	s_mov_b32 m0, s52
	s_nop 0
	global_load_lds_dwordx4 v240, s[46:47]
	s_mov_b32 m0, s53
	s_nop 0
	global_load_lds_dwordx4 v240, s[60:61]
	s_waitcnt lgkmcnt(0)
	s_setprio 1
	s_add_i32 s27, s42, 0x8000
	v_mfma_f32_32x32x16_bf16 v[114:129], v[206:209], v[138:141], v[82:97]
	s_and_b32 s27, s27, 0x6000
	s_add_u32 s42, s42, 0x2000
	s_addc_u32 s43, s43, 0
	v_add_u32_e32 v3, s27, v247
	ds_read_b64_tr_b16 v[206:207], v3 offset:49152
	ds_read_b64_tr_b16 v[208:209], v3 offset:49664
	v_add_f32_e32 v4, v69, v67
	v_add_f32_e32 v5, v68, v66
	v_mfma_f32_32x32x16_bf16 v[98:113], v[194:197], v[138:141], v[82:97]
	ds_read_b64_tr_b16 v[194:195], v3 offset:53248
	ds_read_b64_tr_b16 v[196:197], v3 offset:53760
	v_add_f32_e32 v4, v71, v4
	v_add_f32_e32 v5, v70, v5
	v_add_f32_e32 v4, v73, v4
	v_add_f32_e32 v5, v72, v5
	v_mfma_f32_32x32x16_bf16 v[114:129], v[202:205], v[142:145], v[114:129]
	ds_read_b64_tr_b16 v[202:203], v3 offset:50176
	ds_read_b64_tr_b16 v[204:205], v3 offset:50688
	v_add_f32_e32 v4, v75, v4
	v_add_f32_e32 v5, v74, v5
	v_add_f32_e32 v4, v77, v4
	v_add_f32_e32 v5, v76, v5
	v_mfma_f32_32x32x16_bf16 v[98:113], v[186:189], v[142:145], v[98:113]
	ds_read_b64_tr_b16 v[214:215], v3 offset:54272
	ds_read_b64_tr_b16 v[216:217], v3 offset:54784
	v_add_f32_e32 v4, v79, v4
	v_add_f32_e32 v5, v78, v5
	v_add_f32_e32 v4, v81, v4
	v_add_f32_e32 v5, v80, v5
	v_mfma_f32_32x32x16_bf16 v[114:129], v[198:201], v[146:149], v[114:129]
	ds_read_b64_tr_b16 v[210:211], v3 offset:51200
	ds_read_b64_tr_b16 v[212:213], v3 offset:51712
	v_add_f32_e32 v4, v51, v4
	v_add_f32_e32 v5, v50, v5
	v_add_f32_e32 v4, v53, v4
	v_add_f32_e32 v5, v52, v5
	v_mfma_f32_32x32x16_bf16 v[98:113], v[182:185], v[146:149], v[98:113]
	ds_read_b64_tr_b16 v[12:13], v3 offset:55296
	ds_read_b64_tr_b16 v[14:15], v3 offset:55808
	v_add_f32_e32 v4, v55, v4
	v_add_f32_e32 v5, v54, v5
	v_add_f32_e32 v4, v57, v4
	v_add_f32_e32 v5, v56, v5
	v_mfma_f32_32x32x16_bf16 v[114:129], v[190:193], v[150:153], v[114:129]
	ds_read_b64_tr_b16 v[8:9], v3 offset:52224
	ds_read_b64_tr_b16 v[10:11], v3 offset:52736
	v_add_f32_e32 v4, v59, v4
	v_add_f32_e32 v16, v61, v4
	v_add_f32_e32 v4, v58, v5
	v_add_f32_e32 v17, v60, v4
	v_mfma_f32_32x32x16_bf16 v[98:113], v[170:173], v[150:153], v[98:113]
	s_add_u32 s46, s46, s62
	s_addc_u32 s47, s47, s63
	s_and_b32 s64, s26, 3
	ds_read_b64_tr_b16 v[4:5], v3 offset:56320
	ds_read_b64_tr_b16 v[6:7], v3 offset:56832
	v_add_f32_e32 v3, v63, v16
	v_add_f32_e32 v16, v62, v17
	v_add_f32_e32 v3, v65, v3
	v_add_f32_e32 v16, v64, v16
	v_mfma_f32_32x32x16_bf16 v[114:129], v[178:181], v[154:157], v[114:129]
	s_mulk_i32 s64, 0x3000
	s_add_u32 s60, s60, 0x2000
	s_addc_u32 s61, s61, 0
	v_cvt_pk_bf16_f32 v178, v50, v51
	v_cvt_pk_bf16_f32 v179, v52, v53
	v_cvt_pk_bf16_f32 v186, v66, v67
	v_cvt_pk_bf16_f32 v187, v68, v69
	v_mfma_f32_32x32x16_bf16 v[98:113], v[166:169], v[154:157], v[98:113]
	s_add_i32 s52, s64, s91
	s_add_i32 s64, s42, 0x6000
	v_cvt_pk_bf16_f32 v180, v54, v55
	v_cvt_pk_bf16_f32 v181, v56, v57
	v_cvt_pk_bf16_f32 v188, v70, v71
	v_cvt_pk_bf16_f32 v189, v72, v73
	v_mfma_f32_32x32x16_bf16 v[114:129], v[174:177], v[158:161], v[114:129]
	s_and_b32 s64, s64, 0x6000
	s_add_i32 s53, s64, s93
	v_cvt_pk_bf16_f32 v218, v58, v59
	v_cvt_pk_bf16_f32 v219, v60, v61
	v_cvt_pk_bf16_f32 v182, v74, v75
	v_cvt_pk_bf16_f32 v183, v76, v77
	v_mfma_f32_32x32x16_bf16 v[98:113], v[162:165], v[158:161], v[98:113]
	v_cvt_pk_bf16_f32 v220, v62, v63
	v_cvt_pk_bf16_f32 v221, v64, v65
	v_cvt_pk_bf16_f32 v184, v78, v79
	v_cvt_pk_bf16_f32 v185, v80, v81
	v_add_f32_e32 v3, v3, v16
	v_add_f32_e32 v246, v246, v3
	s_waitcnt vmcnt(3)
	s_waitcnt lgkmcnt(0)
	s_barrier
	s_setprio 0
	v_mfma_f32_32x32x16_bf16 v[18:33], v[186:189], v[206:209], v[18:33]
	s_add_i32 s27, s26, 1
	s_and_b32 s64, s27, 3
	s_mulk_i32 s64, 0x3000
	v_exp_f32_e32 v66, v114
	v_exp_f32_e32 v67, v115
	v_exp_f32_e32 v68, v116
	v_exp_f32_e32 v69, v117
	v_add_u32_e32 v3, s64, v248
	v_mfma_f32_32x32x16_bf16 v[34:49], v[186:189], v[194:197], v[34:49]
	v_exp_f32_e32 v70, v118
	v_exp_f32_e32 v71, v119
	v_exp_f32_e32 v72, v120
	v_exp_f32_e32 v73, v121
	ds_read_b128 v[206:209], v3
	ds_read_b128 v[194:197], v3 offset:512
	v_mfma_f32_32x32x16_bf16 v[18:33], v[182:185], v[202:205], v[18:33]
	v_exp_f32_e32 v74, v122
	v_exp_f32_e32 v75, v123
	v_exp_f32_e32 v76, v124
	v_exp_f32_e32 v77, v125
	ds_read_b128 v[202:205], v3 offset:2048
	ds_read_b128 v[186:189], v3 offset:2560
	v_mfma_f32_32x32x16_bf16 v[34:49], v[182:185], v[214:217], v[34:49]
	v_exp_f32_e32 v78, v126
	v_exp_f32_e32 v79, v127
	v_exp_f32_e32 v80, v128
	v_exp_f32_e32 v81, v129
	ds_read_b128 v[198:201], v3 offset:4096
	ds_read_b128 v[182:185], v3 offset:4608
	v_mfma_f32_32x32x16_bf16 v[18:33], v[178:181], v[210:213], v[18:33]
	v_exp_f32_e32 v50, v98
	v_exp_f32_e32 v51, v99
	v_exp_f32_e32 v52, v100
	v_exp_f32_e32 v53, v101
	ds_read_b128 v[190:193], v3 offset:6144
	ds_read_b128 v[170:173], v3 offset:6656
	v_mfma_f32_32x32x16_bf16 v[34:49], v[178:181], v[12:15], v[34:49]
	v_exp_f32_e32 v54, v102
	v_exp_f32_e32 v55, v103
	v_exp_f32_e32 v56, v104
	v_exp_f32_e32 v57, v105
	ds_read_b128 v[178:181], v3 offset:8192
	ds_read_b128 v[166:169], v3 offset:8704
	v_mfma_f32_32x32x16_bf16 v[18:33], v[218:221], v[8:11], v[18:33]
	v_exp_f32_e32 v58, v106
	v_exp_f32_e32 v59, v107
	v_exp_f32_e32 v60, v108
	v_exp_f32_e32 v61, v109
	ds_read_b128 v[174:177], v3 offset:10240
	ds_read_b128 v[162:165], v3 offset:10752
	v_mfma_f32_32x32x16_bf16 v[34:49], v[218:221], v[4:7], v[34:49]
	v_exp_f32_e32 v62, v110
	v_exp_f32_e32 v63, v111
	v_exp_f32_e32 v64, v112
	v_exp_f32_e32 v65, v113
	s_mov_b32 s26, s27
	s_cmp_eq_u32 s27, s96
	s_cbranch_scc1 .Lmla_ss2_xdone
	s_add_i32 s64, s27, 3
	s_cmp_lt_u32 s64, s94
	s_cbranch_scc1 .Lmla_ss2_top
	s_branch .Lmla_ss_back

; #define ISSUE_K(t, sl) do { glds16(Kg + (long)(t) * (KSLOT / 2), (unsigned)__builtin_amdgcn_readfirstlane(kdst + (sl) * KSLOT)); \
;         if (k2) glds16(Kg + (long)(t) * (KSLOT / 2) + 4096, (unsigned)__builtin_amdgcn_readfirstlane(kdst + (sl) * KSLOT + 8192)); } while (0)
; #define ISSUE_V(t, sl) glds16(Vg + (long)(t) * 4096, (unsigned)__builtin_amdgcn_readfirstlane(vdst + (sl) * VSLOT))
; #define SFENCE() __builtin_amdgcn_sched_barrier(0)
; template <bool FOX>
; __device__ __forceinline__ void attn_unit(const Args& A, int b, int h, int qb, LAS char* shm, LAS float* dg) {
;     ...
;     const int t_end = (tw_last - t0 + 2 < nti) ? tw_last - t0 + 2 : nti;
; #pragma unroll 1
;     for (int t = 1; t < t_end; ++t) {
;         if (t == 1 && 4 < nti) ISSUE_K(t0 + 4, 0);
;         if (t + 4 < nti) ISSUE_K(t0 + t + 4, t % NS);
;         if (t + 2 < nti) ISSUE_V(t0 + t + 2, (t + 2) % NS);
;         SFENCE();
.Lmla_ss_back:
	s_setprio 0
	v_mov_b32_e32 v235, s47
	v_add_co_u32_e32 v234, vcc, s46, v240
	s_nop 1
	v_addc_co_u32_e32 v235, vcc, 0, v235, vcc
	s_mov_b32 s98, 1
	s_waitcnt lgkmcnt(0)
	s_mov_b64 s[60:61], 0
	s_branch .LBB0_825
.Lmla_ss_done:
	s_setprio 0
	v_mov_b32_e32 v235, s47
	v_add_co_u32_e32 v234, vcc, s46, v240
	s_nop 1
	v_addc_co_u32_e32 v235, vcc, 0, v235, vcc
	s_mov_b32 s98, 1
	s_waitcnt lgkmcnt(0)
	s_mov_b64 s[46:47], -1
	s_mov_b64 s[52:53], -1
	s_mov_b64 s[60:61], 0
	s_branch .LBB0_867
